# ping-pong: all MLA tile DMA issue moved into the softmax (VALU) phases, per-phase vmcnt waits
# speedup vs baseline: 1.0171x; 1.0048x over previous
.LBB0_1238:
	s_add_i32 s98, s10, -3
	s_and_b32 s98, s98, 2
	s_mulk_i32 s98, 0x6000
	v_add_u32_e32 v144, s98, v147
	ds_read_b128 v[64:67], v144
	ds_read_b128 v[68:71], v144 offset:12288
	v_add_u32_e32 v146, s98, v148
	v_add_u32_e32 v159, s98, v149
	v_add_u32_e32 v168, s98, v150
	ds_read_b128 v[160:163], v146
	ds_read_b128 v[164:167], v146 offset:12288
	ds_read_b128 v[176:179], v159
	ds_read_b128 v[204:207], v159 offset:12288
	ds_read_b128 v[208:211], v168
	ds_read_b128 v[212:215], v168 offset:12288
	s_add_i32 s13, s10, -1
	s_cmp_lg_u32 s101, 0
	s_cbranch_scc0 .Lhdr_slow
	s_add_i32 s14, s10, -3
	s_branch .LBB0_1242
.Lhdr_slow:
	s_cmp_ge_u32 s13, s9
	s_cbranch_scc1 .LBB0_1240
	s_and_b32 s14, s13, 2
	s_mulk_i32 s14, 0x6000
	s_add_i32 s14, s88, s14
	s_mov_b32 m0, s14
	v_lshl_add_u64 v[240:241], v[174:175], 0, v[180:181]
	global_load_lds_dwordx4 v[174:175], off
	s_add_i32 m0, s14, 0x2000
	v_mov_b32_e32 v185, v181
	global_load_lds_dwordx4 v[172:173], off
	s_add_i32 m0, s14, 0x4000
	v_lshl_add_u64 v[242:243], v[172:173], 0, v[184:185]
	v_mov_b32_e32 v187, v181
	global_load_lds_dwordx4 v[188:189], off
	v_lshl_add_u64 v[244:245], v[188:189], 0, v[186:187]
	v_lshl_add_u64 v[174:175], v[240:241], 0, v[180:181]
	v_lshl_add_u64 v[172:173], v[242:243], 0, v[184:185]
	v_lshl_add_u64 v[188:189], v[244:245], 0, v[186:187]
	s_cmp_lg_u32 s101, 0
	s_cbranch_scc1 .LBB0_1240
	s_and_b32 s14, s10, 3
	s_mulk_i32 s14, 0x6000
	s_add_i32 s14, s88, s14
	s_mov_b32 m0, s14
	s_nop 0
	global_load_lds_dwordx4 v[240:241], off
	s_add_i32 m0, s14, 0x2000
	s_nop 0
	global_load_lds_dwordx4 v[242:243], off
	s_add_i32 m0, s14, 0x4000
	s_nop 0
	global_load_lds_dwordx4 v[244:245], off

.LBB0_1242:
	s_and_b32 s14, s14, 2
	s_mulk_i32 s14, 0x6000
	s_waitcnt lgkmcnt(6)
	v_mfma_f32_32x32x16_bf16 v[80:95], v[64:67], v[112:115], 0
	v_mfma_f32_32x32x16_bf16 v[64:79], v[68:71], v[112:115], 0
	s_waitcnt lgkmcnt(4)
	v_mfma_f32_32x32x16_bf16 v[80:95], v[160:163], v[116:119], v[80:95]
	ds_read_b128 v[160:163], v144 offset:128
	ds_read_b128 v[216:219], v144 offset:12416
	v_mfma_f32_32x32x16_bf16 v[64:79], v[164:167], v[116:119], v[64:79]
	s_waitcnt lgkmcnt(4)
	v_mfma_f32_32x32x16_bf16 v[80:95], v[176:179], v[120:123], v[80:95]
	ds_read_b128 v[164:167], v146 offset:128
	ds_read_b128 v[176:179], v146 offset:12416
	v_mfma_f32_32x32x16_bf16 v[64:79], v[204:207], v[120:123], v[64:79]
	s_waitcnt lgkmcnt(4)
	v_mfma_f32_32x32x16_bf16 v[80:95], v[208:211], v[124:127], v[80:95]
	ds_read_b128 v[204:207], v159 offset:128
	ds_read_b128 v[208:211], v159 offset:12416
	v_mfma_f32_32x32x16_bf16 v[64:79], v[212:215], v[124:127], v[64:79]
	s_waitcnt lgkmcnt(4)
	v_mfma_f32_32x32x16_bf16 v[80:95], v[160:163], v[96:99], v[80:95]
	ds_read_b128 v[160:163], v168 offset:128
	ds_read_b128 v[212:215], v168 offset:12416
	v_mfma_f32_32x32x16_bf16 v[64:79], v[216:219], v[96:99], v[64:79]
	s_waitcnt lgkmcnt(4)
	v_mfma_f32_32x32x16_bf16 v[80:95], v[164:167], v[100:103], v[80:95]
	ds_read_b128 v[164:167], v144 offset:256
	ds_read_b128 v[216:219], v144 offset:12544
	v_mfma_f32_32x32x16_bf16 v[64:79], v[176:179], v[100:103], v[64:79]
	s_waitcnt lgkmcnt(4)
	v_mfma_f32_32x32x16_bf16 v[80:95], v[204:207], v[104:107], v[80:95]
	ds_read_b128 v[176:179], v146 offset:256
	ds_read_b128 v[204:207], v146 offset:12544
	v_mfma_f32_32x32x16_bf16 v[64:79], v[208:211], v[104:107], v[64:79]
	s_waitcnt lgkmcnt(4)
	v_mfma_f32_32x32x16_bf16 v[80:95], v[160:163], v[108:111], v[80:95]
	ds_read_b128 v[160:163], v159 offset:256
	ds_read_b128 v[208:211], v159 offset:12544
	v_mfma_f32_32x32x16_bf16 v[64:79], v[212:215], v[108:111], v[64:79]
	s_waitcnt lgkmcnt(4)
	v_mfma_f32_32x32x16_bf16 v[80:95], v[164:167], v[128:131], v[80:95]
	ds_read_b128 v[164:167], v168 offset:256
	ds_read_b128 v[212:215], v168 offset:12544
	v_mfma_f32_32x32x16_bf16 v[64:79], v[216:219], v[128:131], v[64:79]
	s_waitcnt lgkmcnt(4)
	v_mfma_f32_32x32x16_bf16 v[80:95], v[176:179], v[132:135], v[80:95]
	v_mfma_f32_32x32x16_bf16 v[64:79], v[204:207], v[132:135], v[64:79]
	s_waitcnt lgkmcnt(2)
	v_mfma_f32_32x32x16_bf16 v[80:95], v[160:163], v[136:139], v[80:95]
	v_mfma_f32_32x32x16_bf16 v[64:79], v[208:211], v[136:139], v[64:79]
	s_waitcnt lgkmcnt(0)
	v_mfma_f32_32x32x16_bf16 v[80:95], v[164:167], v[140:143], v[80:95]
	v_mfma_f32_32x32x16_bf16 v[64:79], v[212:215], v[140:143], v[64:79]
	s_cmp_eq_u32 s101, 0
	s_cbranch_scc1 .Lp1_nowait
	s_waitcnt vmcnt(0)
.Lp1_nowait:
	s_barrier
	s_sub_i32 s15, s7, 64
	s_cmp_le_u32 s15, s44
	s_cbranch_scc1 .LBB0_1244
	v_add_u32_e32 v144, 123, v156
	v_cmp_le_i32_e64 s[16:17], 0, v144
	v_cmp_le_i32_e64 s[18:19], 32, v144
	v_cmp_le_i32_e64 vcc, 1, v144
	s_nop 4
	v_cndmask_b32_e64 v80, v199, v80, s[16:17]
	v_cmp_le_i32_e64 s[16:17], 33, v144
	v_cndmask_b32_e64 v64, v199, v64, s[18:19]
	v_cmp_le_i32_e64 s[18:19], 2, v144
	v_cndmask_b32_e64 v81, v199, v81, vcc
	v_cmp_le_i32_e64 vcc, 34, v144
	v_cndmask_b32_e64 v65, v199, v65, s[16:17]
	v_cmp_le_i32_e64 s[16:17], 3, v144
	v_cndmask_b32_e64 v82, v199, v82, s[18:19]
	v_cmp_le_i32_e64 s[18:19], 35, v144
	v_cndmask_b32_e64 v66, v199, v66, vcc
	v_cmp_le_i32_e64 vcc, 8, v144
	v_cndmask_b32_e64 v83, v199, v83, s[16:17]
	v_cmp_le_i32_e64 s[16:17], 40, v144
	v_cndmask_b32_e64 v67, v199, v67, s[18:19]
	v_cmp_le_i32_e64 s[18:19], 9, v144
	v_cndmask_b32_e64 v84, v199, v84, vcc
	v_cmp_le_i32_e64 vcc, 41, v144
	v_cndmask_b32_e64 v68, v199, v68, s[16:17]
	v_cmp_le_i32_e64 s[16:17], 10, v144
	v_cndmask_b32_e64 v85, v199, v85, s[18:19]
	v_cmp_le_i32_e64 s[18:19], 42, v144
	v_cndmask_b32_e64 v69, v199, v69, vcc
	v_cmp_le_i32_e64 vcc, 11, v144
	v_cndmask_b32_e64 v86, v199, v86, s[16:17]
	v_cmp_le_i32_e64 s[16:17], 43, v144
	v_cndmask_b32_e64 v70, v199, v70, s[18:19]
	v_cmp_le_i32_e64 s[18:19], 16, v144
	v_cndmask_b32_e64 v87, v199, v87, vcc
	v_cmp_le_i32_e64 vcc, 48, v144
	v_cndmask_b32_e64 v71, v199, v71, s[16:17]
	v_cmp_le_i32_e64 s[16:17], 17, v144
	v_cndmask_b32_e64 v88, v199, v88, s[18:19]
	v_cmp_le_i32_e64 s[18:19], 49, v144
	v_cndmask_b32_e64 v72, v199, v72, vcc
	v_cmp_le_i32_e64 vcc, 18, v144
	v_cndmask_b32_e64 v89, v199, v89, s[16:17]
	v_cmp_le_i32_e64 s[16:17], 50, v144
	v_cndmask_b32_e64 v73, v199, v73, s[18:19]
	v_cmp_le_i32_e64 s[18:19], 19, v144
	v_cndmask_b32_e64 v90, v199, v90, vcc
	v_cmp_le_i32_e64 vcc, 51, v144
	v_cndmask_b32_e64 v74, v199, v74, s[16:17]
	v_cmp_le_i32_e64 s[16:17], 24, v144
	v_cndmask_b32_e64 v91, v199, v91, s[18:19]
	v_cmp_le_i32_e64 s[18:19], 56, v144
	v_cndmask_b32_e64 v75, v199, v75, vcc
	v_cmp_le_i32_e64 vcc, 25, v144
	v_cndmask_b32_e64 v92, v199, v92, s[16:17]
	v_cmp_le_i32_e64 s[16:17], 57, v144
	v_cndmask_b32_e64 v76, v199, v76, s[18:19]
	v_cmp_le_i32_e64 s[18:19], 26, v144
	v_cndmask_b32_e64 v93, v199, v93, vcc
	v_cmp_le_i32_e64 vcc, 58, v144
	v_cndmask_b32_e64 v77, v199, v77, s[16:17]
	v_cmp_le_i32_e64 s[16:17], 27, v144
	v_cndmask_b32_e64 v94, v199, v94, s[18:19]
	v_cmp_le_i32_e64 s[18:19], 59, v144
	v_cndmask_b32_e64 v78, v199, v78, vcc
	v_cndmask_b32_e64 v95, v199, v95, s[16:17]
	v_cndmask_b32_e64 v79, v199, v79, s[18:19]

.Lf_a:
	s_cmp_ge_u32 s13, s9
	s_cbranch_scc1 .Lno_aload
	s_and_b32 s15, s13, 2
	s_mulk_i32 s15, 0x6000
	s_add_i32 s15, s88, s15
	s_mov_b32 m0, s15
	v_mov_b32_e32 v185, v181
	v_mov_b32_e32 v187, v181
	global_load_lds_dwordx4 v[174:175], off
	s_add_i32 m0, s15, 0x2000
	v_lshl_add_u64 v[174:175], v[174:175], 0, v[180:181]
	global_load_lds_dwordx4 v[172:173], off
	s_add_i32 m0, s15, 0x4000
	v_lshl_add_u64 v[172:173], v[172:173], 0, v[184:185]
	global_load_lds_dwordx4 v[188:189], off
	v_lshl_add_u64 v[188:189], v[188:189], 0, v[186:187]
.Lno_aload:
	s_add_i32 s15, s10, -3
	s_cmp_gt_u32 s15, 3
	s_cselect_b64 s[16:17], -1, 0
	s_xor_b64 s[18:19], s[62:63], -1
	s_or_b64 s[16:17], s[18:19], s[16:17]
	s_and_b64 vcc, exec, s[16:17]
	s_cbranch_vccnz .Lno_bload
	s_add_i32 s15, s11, -3
	v_subrev_u32_e32 v224, 24, v155
	v_xor_b32_e32 v226, s15, v183
	v_mad_i64_i32 v[224:225], s[16:17], s20, v224, 0
	v_lshlrev_b32_e32 v226, 4, v226
	v_lshl_add_u64 v[224:225], v[224:225], 2, s[4:5]
	v_and_b32_e32 v226, 0x70, v226
	v_mov_b32_e32 v227, v181
	v_lshl_add_u64 v[224:225], v[224:225], 0, v[226:227]
	s_add_i32 m0, s12, 0xfffff400
	s_add_i32 s15, s11, -2
	global_load_lds_dwordx4 v[224:225], off nt
	v_add_u32_e32 v224, -16, v155
	v_xor_b32_e32 v226, s15, v183
	v_mad_i64_i32 v[224:225], s[16:17], s20, v224, 0
	v_lshlrev_b32_e32 v226, 4, v226
	v_lshl_add_u64 v[224:225], v[224:225], 2, s[4:5]
	v_and_b32_e32 v226, 0x70, v226
	v_lshl_add_u64 v[224:225], v[224:225], 0, v[226:227]
	s_add_i32 m0, s12, 0xfffff800
	s_add_i32 s15, s11, -1
	global_load_lds_dwordx4 v[224:225], off nt
	v_add_u32_e32 v224, -8, v155
	v_xor_b32_e32 v226, s15, v183
	v_mad_i64_i32 v[224:225], s[16:17], s20, v224, 0
	v_lshlrev_b32_e32 v226, 4, v226
	v_lshl_add_u64 v[224:225], v[224:225], 2, s[4:5]
	v_and_b32_e32 v226, 0x70, v226
	v_lshl_add_u64 v[224:225], v[224:225], 0, v[226:227]
	s_add_i32 m0, s12, 0xfffffc00
	v_xor_b32_e32 v226, s11, v183
	global_load_lds_dwordx4 v[224:225], off nt
	v_mad_i64_i32 v[224:225], s[16:17], s20, v155, 0
	v_lshlrev_b32_e32 v226, 4, v226
	v_lshl_add_u64 v[224:225], v[224:225], 2, s[4:5]
	v_and_b32_e32 v226, 0x70, v226
	v_lshl_add_u64 v[224:225], v[224:225], 0, v[226:227]
	s_mov_b32 m0, s12
	s_nop 0
	global_load_lds_dwordx4 v[224:225], off nt

.Lf_b:
	s_cmp_ge_u32 s13, s9
	s_cbranch_scc1 .Lno_bload2
	s_and_b32 s15, s10, 3
	s_mulk_i32 s15, 0x6000
	s_add_i32 s15, s88, s15
	s_mov_b32 m0, s15
	v_mov_b32_e32 v185, v181
	v_mov_b32_e32 v187, v181
	global_load_lds_dwordx4 v[174:175], off
	s_add_i32 m0, s15, 0x2000
	v_lshl_add_u64 v[174:175], v[174:175], 0, v[180:181]
	global_load_lds_dwordx4 v[172:173], off
	s_add_i32 m0, s15, 0x4000
	v_lshl_add_u64 v[172:173], v[172:173], 0, v[184:185]
	global_load_lds_dwordx4 v[188:189], off
	v_lshl_add_u64 v[188:189], v[188:189], 0, v[186:187]
.Lno_bload2:
	v_add_u32_e32 v209, s14, v151
	v_add_u32_e32 v210, s14, v152
	v_add_u32_e32 v213, s14, v153
	v_add_u32_e32 v214, s14, v154
	ds_read_b64_tr_b16 v[224:225], v209
	ds_read_b64_tr_b16 v[226:227], v210 offset:768
	ds_read_b64_tr_b16 v[228:229], v209 offset:6144
	ds_read_b64_tr_b16 v[230:231], v210 offset:6912
	ds_read_b64_tr_b16 v[232:233], v209 offset:12288
	ds_read_b64_tr_b16 v[234:235], v210 offset:13056
	ds_read_b64_tr_b16 v[236:237], v209 offset:18432
	ds_read_b64_tr_b16 v[238:239], v210 offset:19200
	ds_read_b64_tr_b16 v[240:241], v213
	ds_read_b64_tr_b16 v[242:243], v214 offset:768
	ds_read_b64_tr_b16 v[244:245], v213 offset:6144
	ds_read_b64_tr_b16 v[246:247], v214 offset:6912
	v_exp_f32_e32 v170, v64
	v_exp_f32_e32 v171, v65
	v_exp_f32_e32 v176, v66
	v_exp_f32_e32 v177, v67
	v_exp_f32_e32 v178, v68
	v_exp_f32_e32 v179, v69
	v_exp_f32_e32 v161, v80
	v_exp_f32_e32 v185, v70
	v_exp_f32_e32 v162, v81
	v_exp_f32_e32 v187, v71
	v_exp_f32_e32 v163, v82
	v_exp_f32_e32 v203, v72
	v_exp_f32_e32 v164, v83
	v_exp_f32_e32 v204, v73
	v_exp_f32_e32 v165, v84
	v_exp_f32_e32 v205, v74
	v_exp_f32_e32 v166, v85
	v_exp_f32_e32 v206, v75
	v_exp_f32_e32 v167, v86
	v_exp_f32_e32 v207, v76
	v_exp_f32_e32 v168, v87
	v_exp_f32_e32 v208, v77
	v_exp_f32_e32 v88, v88
	v_exp_f32_e32 v89, v89
	v_exp_f32_e32 v90, v90
	v_exp_f32_e32 v91, v91
	v_cvt_pk_bf16_f32 v72, v161, v162
	v_cvt_pk_bf16_f32 v73, v165, v166
	v_cvt_pk_bf16_f32 v74, v163, v164
	v_cvt_pk_bf16_f32 v75, v167, v168
	v_exp_f32_e32 v92, v92
	v_exp_f32_e32 v93, v93
	v_exp_f32_e32 v94, v94
	v_exp_f32_e32 v95, v95
	v_exp_f32_e32 v211, v78
	v_mov_b32_e32 v80, v79
	v_cvt_pk_bf16_f32 v76, v88, v89
	v_cvt_pk_bf16_f32 v77, v92, v93
	v_cvt_pk_bf16_f32 v78, v90, v91
	v_cvt_pk_bf16_f32 v79, v94, v95
	v_cvt_pk_bf16_f32 v68, v170, v171
	v_cvt_pk_bf16_f32 v69, v178, v179
	v_cvt_pk_bf16_f32 v70, v176, v177
	v_cvt_pk_bf16_f32 v71, v185, v187
	v_exp_f32_e32 v212, v80
	v_cvt_pk_bf16_f32 v64, v203, v204
	v_cvt_pk_bf16_f32 v65, v207, v208
	v_cvt_pk_bf16_f32 v66, v205, v206
	v_cvt_pk_bf16_f32 v67, v211, v212
	v_add_f32_e32 v158, v158, v159
	s_addk_i32 s12, 0x1000
	s_add_i32 s11, s11, 4
	s_add_i32 s10, s10, 2
	s_addk_i32 s7, 0x80
	v_add_u32_e32 v155, 32, v155
	s_cmp_ge_u32 s13, s9
	v_add_u32_e32 v156, 0xffffff80, v156
	v_add_f32_e32 v84, 0, v161
	v_add_f32_e32 v84, v162, v84
	v_add_f32_e32 v84, v163, v84
	v_add_f32_e32 v84, v164, v84
	v_add_f32_e32 v144, v165, v84
	v_add_f32_e32 v80, v166, v144
	v_add_f32_e32 v80, v167, v80
	v_add_f32_e32 v80, v168, v80
	v_add_f32_e32 v80, v88, v80
	v_add_f32_e32 v88, v89, v80
	v_add_f32_e32 v84, v90, v88
	v_add_f32_e32 v84, v91, v84
	v_add_f32_e32 v84, v92, v84
	v_add_f32_e32 v84, v93, v84
	v_add_f32_e32 v88, v94, v84
	v_add_f32_e32 v80, v95, v88
	v_add_f32_e32 v80, v170, v80
	v_add_f32_e32 v80, v171, v80
	v_add_f32_e32 v80, v176, v80
	v_add_f32_e32 v88, v177, v80
	v_add_f32_e32 v248, v178, v88
	v_add_f32_e32 v249, v179, v248
	v_add_f32_e32 v252, v185, v249
	v_add_f32_e32 v253, v187, v252
	v_add_f32_e32 v84, v203, v253
	v_add_f32_e32 v254, v204, v84
	v_add_f32_e32 v255, v205, v254
	v_add_f32_e32 v248, v206, v255
	v_add_f32_e32 v249, v207, v248
	v_add_f32_e32 v80, v208, v249
	v_add_f32_e32 v252, v211, v80
	v_add_f32_e32 v253, v212, v252
	v_add_f32_e32 v158, v158, v253
	s_waitcnt vmcnt(3)
	s_barrier
	s_waitcnt lgkmcnt(10)
	v_mfma_f32_32x32x16_bf16 v[48:63], v[224:227], v[72:75], v[48:63]
	ds_read_b64_tr_b16 v[224:225], v213 offset:12288
	ds_read_b64_tr_b16 v[226:227], v214 offset:13056
	s_waitcnt lgkmcnt(10)
	v_mfma_f32_32x32x16_bf16 v[48:63], v[228:231], v[76:79], v[48:63]
	ds_read_b64_tr_b16 v[228:229], v213 offset:18432
	ds_read_b64_tr_b16 v[230:231], v214 offset:19200
	s_waitcnt lgkmcnt(10)
	v_mfma_f32_32x32x16_bf16 v[48:63], v[232:235], v[68:71], v[48:63]
	ds_read_b64_tr_b16 v[232:233], v209 offset:128
	ds_read_b64_tr_b16 v[234:235], v210 offset:896
	s_waitcnt lgkmcnt(10)
	v_mfma_f32_32x32x16_bf16 v[48:63], v[236:239], v[64:67], v[48:63]
	ds_read_b64_tr_b16 v[236:237], v209 offset:6272
	ds_read_b64_tr_b16 v[238:239], v210 offset:7040
	s_waitcnt lgkmcnt(10)
	v_mfma_f32_32x32x16_bf16 v[32:47], v[240:243], v[72:75], v[32:47]
	ds_read_b64_tr_b16 v[240:241], v209 offset:12416
	ds_read_b64_tr_b16 v[242:243], v210 offset:13184
	s_waitcnt lgkmcnt(10)
	v_mfma_f32_32x32x16_bf16 v[32:47], v[244:247], v[76:79], v[32:47]
	ds_read_b64_tr_b16 v[244:245], v209 offset:18560
	ds_read_b64_tr_b16 v[246:247], v210 offset:19328
	s_waitcnt lgkmcnt(10)
	v_mfma_f32_32x32x16_bf16 v[32:47], v[224:227], v[68:71], v[32:47]
	ds_read_b64_tr_b16 v[224:225], v213 offset:128
	ds_read_b64_tr_b16 v[226:227], v214 offset:896
	s_waitcnt lgkmcnt(10)
	v_mfma_f32_32x32x16_bf16 v[32:47], v[228:231], v[64:67], v[32:47]
	ds_read_b64_tr_b16 v[228:229], v213 offset:6272
	ds_read_b64_tr_b16 v[230:231], v214 offset:7040
	s_waitcnt lgkmcnt(10)
	v_mfma_f32_32x32x16_bf16 v[0:15], v[232:235], v[72:75], v[0:15]
	ds_read_b64_tr_b16 v[232:233], v213 offset:12416
	ds_read_b64_tr_b16 v[234:235], v214 offset:13184
	s_waitcnt lgkmcnt(10)
	v_mfma_f32_32x32x16_bf16 v[0:15], v[236:239], v[76:79], v[0:15]
	ds_read_b64_tr_b16 v[236:237], v213 offset:18560
	ds_read_b64_tr_b16 v[238:239], v214 offset:19328
	s_waitcnt lgkmcnt(10)
	v_mfma_f32_32x32x16_bf16 v[0:15], v[240:243], v[68:71], v[0:15]
	s_waitcnt lgkmcnt(8)
	v_mfma_f32_32x32x16_bf16 v[0:15], v[244:247], v[64:67], v[0:15]
	s_waitcnt lgkmcnt(6)
	v_mfma_f32_32x32x16_bf16 v[16:31], v[224:227], v[72:75], v[16:31]
	s_waitcnt lgkmcnt(4)
	v_mfma_f32_32x32x16_bf16 v[16:31], v[228:231], v[76:79], v[16:31]
	s_waitcnt lgkmcnt(2)
	v_mfma_f32_32x32x16_bf16 v[16:31], v[232:235], v[68:71], v[16:31]
	s_waitcnt lgkmcnt(0)
	v_mfma_f32_32x32x16_bf16 v[16:31], v[236:239], v[64:67], v[16:31]
	s_barrier
	s_cbranch_scc1 .LBB0_1250
	s_branch .LBB0_1238
.LBB0_1250:
	s_waitcnt vmcnt(0)
	s_cmp_eq_u32 s101, 0
	s_cbranch_scc1 .Lnostag_out
	s_cmp_ge_u32 s88, 0x1000
	s_cbranch_scc1 .Lnostag_out
	s_barrier
